# P1 epilogue Z stores tagged nt (streamed output, keeps GEMM panels in L2)
# speedup vs baseline: 1.0096x; 1.0096x over previous
;     __device__ __forceinline__ void operator()(const f32x4 (&acc)[2][2][4][2], const Unit& u, int wr, int wc, int fr, int fq) const {
;         const int row0 = u.pm * BM + wr * 64 + fr, col0 = u.pn * BM + wc * 32 + 8 * fq;
;         const float tsc = (MODE == 0 && u.pn >= sc_lo && u.pn < sc_hi) ? sc : 1.f;
;         float ra[2][4]; f32x4 cb[2][2];
;         if (QI8) {
; #pragma unroll
;             for (int ai = 0; ai < 2; ++ai)
; #pragma unroll
;                 for (int m = 0; m < 4; ++m) ra[ai][m] = sa[row0 + ai * HALF + m * 16];
; #pragma unroll
;             for (int bj = 0; bj < 2; ++bj) { cb[bj][0] = *(const f32x4*)(sb + col0 + bj * HALF) * tsc; cb[bj][1] = *(const f32x4*)(sb + col0 + bj * HALF + 4) * tsc; } }
;         else if (MODE == 1) {
; #pragma unroll
;             for (int bj = 0; bj < 2; ++bj) { cb[bj][0] = *(const f32x4*)(colscale + col0 + bj * HALF); cb[bj][1] = *(const f32x4*)(colscale + col0 + bj * HALF + 4); } }
;         const bool dual = (MODE == 0) && aux != nullptr && u.pn >= ZC_KV / 256 && u.pn < ZC_KV / 256 + 4;
;         u32x4 gq[2][2], aq[2][2]; f32x4 rs[2][2][2];
;     ...
;         EPB_LOAD(0);
; #pragma unroll
;         for (int kb = 0; kb < 8; ++kb) { const int ai = kb >> 2, m = kb & 3;
;             if (kb < 7) EPB_LOAD(kb + 1);
;             { const int row = row0 + ai * HALF + m * 16; float rmx = 0.f;
; #pragma unroll
;                 for (int bj = 0; bj < 2; ++bj) { const int col = col0 + bj * HALF; f32x4 v0 = acc[ai][bj][m][0], v1 = acc[ai][bj][m][1];
;                     if (QI8) { const f32x4 c0 = cb[bj][0] * ra[ai][m], c1 = cb[bj][1] * ra[ai][m]; const i32x4 i0 = __builtin_bit_cast(i32x4, v0), i1 = __builtin_bit_cast(i32x4, v1);
;                         v0 = (f32x4){(float)i0[0], (float)i0[1], (float)i0[2], (float)i0[3]} * c0; v1 = (f32x4){(float)i1[0], (float)i1[1], (float)i1[2], (float)i1[3]} * c1; }
;                     else if (MODE == 0) { v0 = v0 * tsc; v1 = v1 * tsc; }
;                     if (!QI8 && MODE == 1) { v0 = v0 * cb[bj][0]; v1 = v1 * cb[bj][1]; }
;                     if (MODE == 2 || MODE == 3) { const u32x4 g = gq[kb & 1][bj];
;                         f32x4 g0 = {sigmoidf_(bflo(g.x)), sigmoidf_(bfhi(g.x)), sigmoidf_(bflo(g.y)), sigmoidf_(bfhi(g.y))};
;                         f32x4 g1 = {sigmoidf_(bflo(g.z)), sigmoidf_(bfhi(g.z)), sigmoidf_(bflo(g.w)), sigmoidf_(bfhi(g.w))};
.LBB0_167:
	v_lshl_or_b32 v138, s30, 8, v228
	v_ashrrev_i32_e32 v139, 31, v138
	v_lshl_add_u64 v[134:135], v[138:139], 2, s[16:17]
	global_load_dwordx4 v[166:169], v[134:135], off offset:16
	global_load_dwordx4 v[144:147], v[134:135], off
	s_lshl_b32 s10, s10, 8
	s_add_i32 s23, s10, s63
	v_or_b32_e32 v156, s23, v1
	v_ashrrev_i32_e32 v157, 31, v156
	v_lshl_add_u64 v[140:141], v[156:157], 2, s[4:5]
	global_load_dword v164, v[140:141], off
	global_load_dwordx4 v[130:133], v[134:135], off offset:528
	s_nop 0
	global_load_dwordx4 v[134:137], v[134:135], off offset:512
	s_nop 0
	global_load_dword v162, v[140:141], off offset:64
	global_load_dword v160, v[140:141], off offset:128
	global_load_dword v158, v[140:141], off offset:192
	global_load_dword v154, v[140:141], off offset:512
	global_load_dword v152, v[140:141], off offset:576
	global_load_dword v142, v[140:141], off offset:640
	s_nop 0
	global_load_dword v140, v[140:141], off offset:704
	s_and_b32 s10, s30, -8
	v_readlane_b32 s34, v245, 9
	s_cmp_eq_u32 s10, 8
	v_cvt_f32_i32_e32 v171, v129
	v_cvt_f32_i32_e32 v170, v128
	v_readlane_b32 s35, v245, 10
	s_cselect_b64 vcc, -1, 0
	v_cvt_f32_i32_e32 v127, v127
	v_cvt_f32_i32_e32 v126, v126
	v_cvt_f32_i32_e32 v123, v123
	v_cvt_f32_i32_e32 v122, v122
	v_cvt_f32_i32_e32 v125, v125
	v_cvt_f32_i32_e32 v124, v124
	v_mov_b64_e32 v[148:149], s[34:35]
	v_cndmask_b32_e32 v128, 1.0, v232, vcc
	s_and_b32 s25, s30, -4
	v_mad_i64_i32 v[172:173], s[10:11], v156, s68, v[148:149]
	s_cmp_eq_u32 s25, 16
	s_cselect_b64 s[34:35], -1, 0
	s_ashr_i32 s23, s23, 4
	s_addk_i32 s23, 0xc000
	s_cmp_lg_u32 s25, 16
	s_waitcnt vmcnt(0)
	v_pk_mul_f32 v[148:149], v[128:129], v[146:147] op_sel_hi:[0,1]
	v_pk_mul_f32 v[150:151], v[128:129], v[144:145] op_sel_hi:[0,1]
	v_pk_mul_f32 v[144:145], v[128:129], v[168:169] op_sel_hi:[0,1]
	v_pk_mul_f32 v[146:147], v[128:129], v[166:167] op_sel_hi:[0,1]
	v_pk_mul_f32 v[166:167], v[164:165], v[148:149] op_sel_hi:[0,1]
	v_pk_mul_f32 v[168:169], v[164:165], v[150:151] op_sel_hi:[0,1]
	v_pk_mul_f32 v[174:175], v[164:165], v[144:145] op_sel_hi:[0,1]
	v_pk_mul_f32 v[176:177], v[164:165], v[146:147] op_sel_hi:[0,1]
	v_pk_mul_f32 v[166:167], v[166:167], v[170:171]
	v_pk_mul_f32 v[126:127], v[168:169], v[126:127]
	v_pk_mul_f32 v[168:169], v[174:175], v[124:125]
	v_pk_mul_f32 v[124:125], v[176:177], v[122:123]
	v_cvt_pk_bf16_f32 v122, v126, v127
	v_cvt_pk_bf16_f32 v123, v166, v167
	v_lshl_add_u64 v[166:167], v[138:139], 1, v[172:173]
	v_cvt_pk_bf16_f32 v124, v124, v125
	v_cvt_pk_bf16_f32 v125, v168, v169
	global_store_dwordx4 v[166:167], v[122:125], off nt
	s_cbranch_scc1 .LBB0_169
	s_lshl_b32 s10, s30, 10
	s_add_i32 s10, s23, s10
	s_ashr_i32 s11, s10, 31
	s_lshl_b64 s[10:11], s[10:11], 12
	v_lshl_add_u64 v[126:127], v[206:207], 0, s[10:11]
	global_store_dwordx4 v[126:127], v[122:125], off nt
.LBB0_169:
	v_cvt_f32_i32_e32 v119, v119
	v_cvt_f32_i32_e32 v118, v118
	v_mov_b32_e32 v129, v128
	v_cvt_f32_i32_e32 v115, v115
	v_cvt_f32_i32_e32 v117, v117
	v_cvt_f32_i32_e32 v116, v116
	v_cvt_f32_i32_e32 v114, v114
	v_mov_b32_e32 v165, v164
	v_mov_b32_e32 v122, v128
	v_mov_b32_e32 v123, v128
	v_pk_mul_f32 v[126:127], v[128:129], v[134:135]
	v_pk_mul_f32 v[124:125], v[122:123], v[136:137]
	v_pk_mul_f32 v[122:123], v[122:123], v[132:133]
	v_pk_mul_f32 v[128:129], v[128:129], v[130:131]
	v_mov_b32_e32 v130, v164
	v_mov_b32_e32 v131, v164
	v_pk_mul_f32 v[134:135], v[164:165], v[126:127]
	v_pk_mul_f32 v[132:133], v[130:131], v[124:125]
	v_pk_mul_f32 v[130:131], v[130:131], v[122:123]
	v_pk_mul_f32 v[136:137], v[164:165], v[128:129]
	v_cvt_f32_i32_e32 v121, v121
	v_cvt_f32_i32_e32 v120, v120
	v_pk_mul_f32 v[118:119], v[134:135], v[118:119]
	v_or_b32_e32 v141, 0x80, v138
	v_pk_mul_f32 v[130:131], v[130:131], v[116:117]
	v_pk_mul_f32 v[116:117], v[136:137], v[114:115]
	v_cvt_pk_bf16_f32 v114, v118, v119
	v_cndmask_b32_e64 v118, 0, 1, s[34:35]
	v_cmp_ne_u32_e64 s[10:11], 1, v118
	v_lshlrev_b32_e32 v118, 2, v141
	s_andn2_b64 vcc, exec, s[34:35]
	v_and_b32_e32 v118, 0x4e00, v118
	v_pk_mul_f32 v[120:121], v[132:133], v[120:121]
	s_nop 0
	v_cvt_pk_bf16_f32 v115, v120, v121
	v_cvt_pk_bf16_f32 v116, v116, v117
	v_cvt_pk_bf16_f32 v117, v130, v131
	global_store_dwordx4 v[166:167], v[114:117], off offset:256 nt
	s_cbranch_vccnz .LBB0_171
	v_add_u32_e32 v120, s23, v118
	v_ashrrev_i32_e32 v121, 31, v120
	v_lshlrev_b64 v[120:121], 12, v[120:121]
	v_lshl_add_u64 v[120:121], v[206:207], 0, v[120:121]
	global_store_dwordx4 v[120:121], v[114:117], off nt
.LBB0_171:
	v_cvt_f32_i32_e32 v111, v111
	v_cvt_f32_i32_e32 v110, v110
	v_cvt_f32_i32_e32 v113, v113
	v_cvt_f32_i32_e32 v112, v112
	v_cvt_f32_i32_e32 v107, v107
	v_cvt_f32_i32_e32 v109, v109
	v_cvt_f32_i32_e32 v108, v108
	v_cvt_f32_i32_e32 v106, v106
	v_pk_mul_f32 v[120:121], v[162:163], v[150:151] op_sel_hi:[0,1]
	v_readlane_b32 s34, v245, 9
	v_pk_mul_f32 v[116:117], v[162:163], v[148:149] op_sel_hi:[0,1]
	v_pk_mul_f32 v[130:131], v[162:163], v[144:145] op_sel_hi:[0,1]
	v_pk_mul_f32 v[132:133], v[162:163], v[146:147] op_sel_hi:[0,1]
	v_pk_mul_f32 v[110:111], v[120:121], v[110:111]
	v_readlane_b32 s35, v245, 10
	v_or_b32_e32 v115, 16, v156
	v_pk_mul_f32 v[112:113], v[116:117], v[112:113]
	v_pk_mul_f32 v[116:117], v[130:131], v[108:109]
	v_pk_mul_f32 v[108:109], v[132:133], v[106:107]
	v_cvt_pk_bf16_f32 v106, v110, v111
	v_mov_b64_e32 v[110:111], s[34:35]
	v_ashrrev_i32_e32 v114, 4, v115
	v_mad_i64_i32 v[110:111], s[34:35], v115, s68, v[110:111]
	v_add_u32_e32 v114, 0xffffc000, v114
	v_lshl_add_u64 v[110:111], v[138:139], 1, v[110:111]
	s_and_b64 vcc, exec, s[10:11]
	v_cvt_pk_bf16_f32 v107, v112, v113
	v_cvt_pk_bf16_f32 v108, v108, v109
	v_cvt_pk_bf16_f32 v109, v116, v117
	global_store_dwordx4 v[110:111], v[106:109], off nt
	s_cbranch_vccnz .LBB0_173
	v_lshl_add_u32 v112, s30, 10, v114
	v_ashrrev_i32_e32 v113, 31, v112
	v_lshlrev_b64 v[112:113], 12, v[112:113]
	v_lshl_add_u64 v[112:113], v[206:207], 0, v[112:113]
	global_store_dwordx4 v[112:113], v[106:109], off nt
;     __device__ __forceinline__ void operator()(const f32x4 (&acc)[2][2][4][2], const Unit& u, int wr, int wc, int fr, int fq) const {
;     ...
;         for (int kb = 0; kb < 8; ++kb) { const int ai = kb >> 2, m = kb & 3;
;             if (kb < 7) EPB_LOAD(kb + 1);
;             { const int row = row0 + ai * HALF + m * 16; float rmx = 0.f;
; #pragma unroll
;                 for (int bj = 0; bj < 2; ++bj) { const int col = col0 + bj * HALF; f32x4 v0 = acc[ai][bj][m][0], v1 = acc[ai][bj][m][1];
;                     if (QI8) { const f32x4 c0 = cb[bj][0] * ra[ai][m], c1 = cb[bj][1] * ra[ai][m]; const i32x4 i0 = __builtin_bit_cast(i32x4, v0), i1 = __builtin_bit_cast(i32x4, v1);
;                         v0 = (f32x4){(float)i0[0], (float)i0[1], (float)i0[2], (float)i0[3]} * c0; v1 = (f32x4){(float)i1[0], (float)i1[1], (float)i1[2], (float)i1[3]} * c1; }
;                     else if (MODE == 0) { v0 = v0 * tsc; v1 = v1 * tsc; }
;                     if (!QI8 && MODE == 1) { v0 = v0 * cb[bj][0]; v1 = v1 * cb[bj][1]; }
;                     if (MODE == 2 || MODE == 3) { const u32x4 g = gq[kb & 1][bj];
;                         f32x4 g0 = {sigmoidf_(bflo(g.x)), sigmoidf_(bfhi(g.x)), sigmoidf_(bflo(g.y)), sigmoidf_(bfhi(g.y))};
;                         f32x4 g1 = {sigmoidf_(bflo(g.z)), sigmoidf_(bfhi(g.z)), sigmoidf_(bflo(g.w)), sigmoidf_(bfhi(g.w))};
;                         v0 = v0 * g0; v1 = v1 * g1;
;                         if (MODE == 3) { const u32x4 q = aq[kb & 1][bj];
;                             v0 = v0 + (f32x4){bflo(q.x), bfhi(q.x), bflo(q.y), bfhi(q.y)}; v1 = v1 + (f32x4){bflo(q.z), bfhi(q.z), bflo(q.w), bfhi(q.w)}; } }
;                     if (MODE == 4) { v0 = v0 + rs[kb & 1][bj][0]; v1 = v1 + rs[kb & 1][bj][1]; }
;                     if (MODE == 5) { const u32x4 c = gq[kb & 1][bj], q = aq[kb & 1][bj];
;                         v0 = (f32x4){bflo(c.x) + sigmoidf_(v0[0]) * bflo(q.x), bfhi(c.x) + sigmoidf_(v0[1]) * bfhi(q.x), bflo(c.y) + sigmoidf_(v0[2]) * bflo(q.y), bfhi(c.y) + sigmoidf_(v0[3]) * bfhi(q.y)};
;                         v1 = (f32x4){bflo(c.z) + sigmoidf_(v1[0]) * bflo(q.z), bfhi(c.z) + sigmoidf_(v1[1]) * bfhi(q.z), bflo(c.w) + sigmoidf_(v1[2]) * bflo(q.w), bfhi(c.w) + sigmoidf_(v1[3]) * bfhi(q.w)}; }
;                     u32x4 w; w.x = cvtpk(v0[0], v0[1]); w.y = cvtpk(v0[2], v0[3]); w.z = cvtpk(v1[0], v1[1]); w.w = cvtpk(v1[2], v1[3]);
.LBB0_173:
	v_cvt_f32_i32_e32 v99, v99
	v_cvt_f32_i32_e32 v101, v101
	v_cvt_f32_i32_e32 v100, v100
	v_cvt_f32_i32_e32 v98, v98
	v_cvt_f32_i32_e32 v103, v103
	v_cvt_f32_i32_e32 v102, v102
	v_cvt_f32_i32_e32 v105, v105
	v_cvt_f32_i32_e32 v104, v104
	v_mov_b32_e32 v163, v162
	v_mov_b32_e32 v106, v162
	v_mov_b32_e32 v107, v162
	v_pk_mul_f32 v[108:109], v[106:107], v[124:125]
	v_pk_mul_f32 v[106:107], v[106:107], v[122:123]
	v_pk_mul_f32 v[116:117], v[162:163], v[128:129]
	v_pk_mul_f32 v[112:113], v[162:163], v[126:127]
	v_pk_mul_f32 v[106:107], v[106:107], v[100:101]
	v_pk_mul_f32 v[100:101], v[116:117], v[98:99]
	s_and_b64 vcc, exec, s[10:11]
	v_pk_mul_f32 v[104:105], v[108:109], v[104:105]
	v_pk_mul_f32 v[102:103], v[112:113], v[102:103]
	s_nop 0
	v_cvt_pk_bf16_f32 v98, v102, v103
	v_cvt_pk_bf16_f32 v99, v104, v105
	v_cvt_pk_bf16_f32 v100, v100, v101
	v_cvt_pk_bf16_f32 v101, v106, v107
	global_store_dwordx4 v[110:111], v[98:101], off offset:256 nt
	s_cbranch_vccnz .LBB0_175
	v_add_u32_e32 v102, v114, v118
	v_ashrrev_i32_e32 v103, 31, v102
	v_lshlrev_b64 v[102:103], 12, v[102:103]
	v_lshl_add_u64 v[102:103], v[206:207], 0, v[102:103]
	global_store_dwordx4 v[102:103], v[98:101], off nt
.LBB0_175:
	v_cvt_f32_i32_e32 v95, v95
	v_cvt_f32_i32_e32 v94, v94
	v_cvt_f32_i32_e32 v97, v97
	v_cvt_f32_i32_e32 v96, v96
	v_cvt_f32_i32_e32 v91, v91
	v_cvt_f32_i32_e32 v93, v93
	v_cvt_f32_i32_e32 v92, v92
	v_cvt_f32_i32_e32 v90, v90
	v_pk_mul_f32 v[102:103], v[160:161], v[150:151] op_sel_hi:[0,1]
	v_readlane_b32 s34, v245, 9
	v_pk_mul_f32 v[100:101], v[160:161], v[148:149] op_sel_hi:[0,1]
	v_pk_mul_f32 v[104:105], v[160:161], v[144:145] op_sel_hi:[0,1]
	v_pk_mul_f32 v[106:107], v[160:161], v[146:147] op_sel_hi:[0,1]
	v_pk_mul_f32 v[94:95], v[102:103], v[94:95]
	v_readlane_b32 s35, v245, 10
	v_or_b32_e32 v99, 32, v156
	v_pk_mul_f32 v[96:97], v[100:101], v[96:97]
	v_pk_mul_f32 v[100:101], v[104:105], v[92:93]
	v_pk_mul_f32 v[92:93], v[106:107], v[90:91]
	v_cvt_pk_bf16_f32 v90, v94, v95
	v_mov_b64_e32 v[94:95], s[34:35]
	v_ashrrev_i32_e32 v98, 4, v99
	v_mad_i64_i32 v[94:95], s[34:35], v99, s68, v[94:95]
	v_add_u32_e32 v98, 0xffffc000, v98
	v_lshl_add_u64 v[94:95], v[138:139], 1, v[94:95]
	s_and_b64 vcc, exec, s[10:11]
	v_cvt_pk_bf16_f32 v91, v96, v97
	v_cvt_pk_bf16_f32 v92, v92, v93
	v_cvt_pk_bf16_f32 v93, v100, v101
	global_store_dwordx4 v[94:95], v[90:93], off nt
	s_cbranch_vccnz .LBB0_177
	v_lshl_add_u32 v96, s30, 10, v98
	v_ashrrev_i32_e32 v97, 31, v96
	v_lshlrev_b64 v[96:97], 12, v[96:97]
	v_lshl_add_u64 v[96:97], v[206:207], 0, v[96:97]
	global_store_dwordx4 v[96:97], v[90:93], off nt
.LBB0_177:
	v_cvt_f32_i32_e32 v83, v83
	v_cvt_f32_i32_e32 v85, v85
	v_cvt_f32_i32_e32 v84, v84
	v_cvt_f32_i32_e32 v82, v82
	v_cvt_f32_i32_e32 v87, v87
	v_cvt_f32_i32_e32 v86, v86
	v_cvt_f32_i32_e32 v89, v89
	v_cvt_f32_i32_e32 v88, v88
	v_mov_b32_e32 v161, v160
	v_mov_b32_e32 v90, v160
	v_mov_b32_e32 v91, v160
	v_pk_mul_f32 v[92:93], v[90:91], v[124:125]
	v_pk_mul_f32 v[90:91], v[90:91], v[122:123]
	v_pk_mul_f32 v[100:101], v[160:161], v[128:129]
	v_pk_mul_f32 v[96:97], v[160:161], v[126:127]
	v_pk_mul_f32 v[90:91], v[90:91], v[84:85]
	v_pk_mul_f32 v[84:85], v[100:101], v[82:83]
	s_and_b64 vcc, exec, s[10:11]
	v_pk_mul_f32 v[88:89], v[92:93], v[88:89]
	v_pk_mul_f32 v[86:87], v[96:97], v[86:87]
	s_nop 0
	v_cvt_pk_bf16_f32 v82, v86, v87
	v_cvt_pk_bf16_f32 v83, v88, v89
	v_cvt_pk_bf16_f32 v84, v84, v85
	v_cvt_pk_bf16_f32 v85, v90, v91
	global_store_dwordx4 v[94:95], v[82:85], off offset:256 nt
	s_cbranch_vccnz .LBB0_179
	v_add_u32_e32 v86, v98, v118
	v_ashrrev_i32_e32 v87, 31, v86
	v_lshlrev_b64 v[86:87], 12, v[86:87]
	v_lshl_add_u64 v[86:87], v[206:207], 0, v[86:87]
	global_store_dwordx4 v[86:87], v[82:85], off nt
.LBB0_179:
	v_cvt_f32_i32_e32 v79, v79
	v_cvt_f32_i32_e32 v78, v78
	v_cvt_f32_i32_e32 v81, v81
	v_cvt_f32_i32_e32 v80, v80
	v_cvt_f32_i32_e32 v75, v75
	v_cvt_f32_i32_e32 v77, v77
	v_cvt_f32_i32_e32 v76, v76
	v_cvt_f32_i32_e32 v74, v74
	v_pk_mul_f32 v[86:87], v[158:159], v[150:151] op_sel_hi:[0,1]
	v_readlane_b32 s34, v245, 9
	v_pk_mul_f32 v[84:85], v[158:159], v[148:149] op_sel_hi:[0,1]
	v_pk_mul_f32 v[88:89], v[158:159], v[144:145] op_sel_hi:[0,1]
	v_pk_mul_f32 v[90:91], v[158:159], v[146:147] op_sel_hi:[0,1]
	v_pk_mul_f32 v[78:79], v[86:87], v[78:79]
	v_readlane_b32 s35, v245, 10
	v_or_b32_e32 v83, 48, v156
	v_pk_mul_f32 v[80:81], v[84:85], v[80:81]
	v_pk_mul_f32 v[84:85], v[88:89], v[76:77]
	v_pk_mul_f32 v[76:77], v[90:91], v[74:75]
	v_cvt_pk_bf16_f32 v74, v78, v79
	v_mov_b64_e32 v[78:79], s[34:35]
	v_ashrrev_i32_e32 v82, 4, v83
	v_mad_i64_i32 v[78:79], s[34:35], v83, s68, v[78:79]
	v_add_u32_e32 v82, 0xffffc000, v82
	v_lshl_add_u64 v[78:79], v[138:139], 1, v[78:79]
	s_and_b64 vcc, exec, s[10:11]
	v_cvt_pk_bf16_f32 v75, v80, v81
	v_cvt_pk_bf16_f32 v76, v76, v77
	v_cvt_pk_bf16_f32 v77, v84, v85
	global_store_dwordx4 v[78:79], v[74:77], off nt
	s_cbranch_vccnz .LBB0_181
	v_lshl_add_u32 v80, s30, 10, v82
	v_ashrrev_i32_e32 v81, 31, v80
	v_lshlrev_b64 v[80:81], 12, v[80:81]
	v_lshl_add_u64 v[80:81], v[206:207], 0, v[80:81]
	global_store_dwordx4 v[80:81], v[74:77], off nt
;     __device__ __forceinline__ void operator()(const f32x4 (&acc)[2][2][4][2], const Unit& u, int wr, int wc, int fr, int fq) const {
;     ...
;         for (int kb = 0; kb < 8; ++kb) { const int ai = kb >> 2, m = kb & 3;
;             if (kb < 7) EPB_LOAD(kb + 1);
;             { const int row = row0 + ai * HALF + m * 16; float rmx = 0.f;
; #pragma unroll
;                 for (int bj = 0; bj < 2; ++bj) { const int col = col0 + bj * HALF; f32x4 v0 = acc[ai][bj][m][0], v1 = acc[ai][bj][m][1];
;                     if (QI8) { const f32x4 c0 = cb[bj][0] * ra[ai][m], c1 = cb[bj][1] * ra[ai][m]; const i32x4 i0 = __builtin_bit_cast(i32x4, v0), i1 = __builtin_bit_cast(i32x4, v1);
;                         v0 = (f32x4){(float)i0[0], (float)i0[1], (float)i0[2], (float)i0[3]} * c0; v1 = (f32x4){(float)i1[0], (float)i1[1], (float)i1[2], (float)i1[3]} * c1; }
;                     else if (MODE == 0) { v0 = v0 * tsc; v1 = v1 * tsc; }
;                     if (!QI8 && MODE == 1) { v0 = v0 * cb[bj][0]; v1 = v1 * cb[bj][1]; }
;                     if (MODE == 2 || MODE == 3) { const u32x4 g = gq[kb & 1][bj];
;                         f32x4 g0 = {sigmoidf_(bflo(g.x)), sigmoidf_(bfhi(g.x)), sigmoidf_(bflo(g.y)), sigmoidf_(bfhi(g.y))};
;                         f32x4 g1 = {sigmoidf_(bflo(g.z)), sigmoidf_(bfhi(g.z)), sigmoidf_(bflo(g.w)), sigmoidf_(bfhi(g.w))};
;                         v0 = v0 * g0; v1 = v1 * g1;
;                         if (MODE == 3) { const u32x4 q = aq[kb & 1][bj];
;                             v0 = v0 + (f32x4){bflo(q.x), bfhi(q.x), bflo(q.y), bfhi(q.y)}; v1 = v1 + (f32x4){bflo(q.z), bfhi(q.z), bflo(q.w), bfhi(q.w)}; } }
;                     if (MODE == 4) { v0 = v0 + rs[kb & 1][bj][0]; v1 = v1 + rs[kb & 1][bj][1]; }
;                     if (MODE == 5) { const u32x4 c = gq[kb & 1][bj], q = aq[kb & 1][bj];
;                         v0 = (f32x4){bflo(c.x) + sigmoidf_(v0[0]) * bflo(q.x), bfhi(c.x) + sigmoidf_(v0[1]) * bfhi(q.x), bflo(c.y) + sigmoidf_(v0[2]) * bflo(q.y), bfhi(c.y) + sigmoidf_(v0[3]) * bfhi(q.y)};
;                         v1 = (f32x4){bflo(c.z) + sigmoidf_(v1[0]) * bflo(q.z), bfhi(c.z) + sigmoidf_(v1[1]) * bfhi(q.z), bflo(c.w) + sigmoidf_(v1[2]) * bflo(q.w), bfhi(c.w) + sigmoidf_(v1[3]) * bfhi(q.w)}; }
;                     u32x4 w; w.x = cvtpk(v0[0], v0[1]); w.y = cvtpk(v0[2], v0[3]); w.z = cvtpk(v1[0], v1[1]); w.w = cvtpk(v1[2], v1[3]);
.LBB0_181:
	v_cvt_f32_i32_e32 v67, v67
	v_cvt_f32_i32_e32 v69, v69
	v_cvt_f32_i32_e32 v68, v68
	v_cvt_f32_i32_e32 v66, v66
	v_cvt_f32_i32_e32 v71, v71
	v_cvt_f32_i32_e32 v70, v70
	v_cvt_f32_i32_e32 v73, v73
	v_cvt_f32_i32_e32 v72, v72
	v_mov_b32_e32 v159, v158
	v_mov_b32_e32 v74, v158
	v_mov_b32_e32 v75, v158
	v_pk_mul_f32 v[76:77], v[74:75], v[124:125]
	v_pk_mul_f32 v[74:75], v[74:75], v[122:123]
	v_pk_mul_f32 v[84:85], v[158:159], v[128:129]
	v_pk_mul_f32 v[80:81], v[158:159], v[126:127]
	v_pk_mul_f32 v[74:75], v[74:75], v[68:69]
	v_pk_mul_f32 v[68:69], v[84:85], v[66:67]
	s_and_b64 vcc, exec, s[10:11]
	v_pk_mul_f32 v[72:73], v[76:77], v[72:73]
	v_pk_mul_f32 v[70:71], v[80:81], v[70:71]
	s_nop 0
	v_cvt_pk_bf16_f32 v66, v70, v71
	v_cvt_pk_bf16_f32 v67, v72, v73
	v_cvt_pk_bf16_f32 v68, v68, v69
	v_cvt_pk_bf16_f32 v69, v74, v75
	global_store_dwordx4 v[78:79], v[66:69], off offset:256 nt
	s_cbranch_vccnz .LBB0_183
	v_add_u32_e32 v70, v82, v118
	v_ashrrev_i32_e32 v71, 31, v70
	v_lshlrev_b64 v[70:71], 12, v[70:71]
	v_lshl_add_u64 v[70:71], v[206:207], 0, v[70:71]
	global_store_dwordx4 v[70:71], v[66:69], off nt
.LBB0_183:
	v_cvt_f32_i32_e32 v63, v63
	v_cvt_f32_i32_e32 v62, v62
	v_cvt_f32_i32_e32 v65, v65
	v_cvt_f32_i32_e32 v64, v64
	v_cvt_f32_i32_e32 v59, v59
	v_cvt_f32_i32_e32 v61, v61
	v_cvt_f32_i32_e32 v60, v60
	v_cvt_f32_i32_e32 v58, v58
	v_pk_mul_f32 v[70:71], v[154:155], v[150:151] op_sel_hi:[0,1]
	v_readlane_b32 s34, v245, 9
	v_pk_mul_f32 v[68:69], v[154:155], v[148:149] op_sel_hi:[0,1]
	v_pk_mul_f32 v[72:73], v[154:155], v[144:145] op_sel_hi:[0,1]
	v_pk_mul_f32 v[74:75], v[154:155], v[146:147] op_sel_hi:[0,1]
	v_pk_mul_f32 v[62:63], v[70:71], v[62:63]
	v_readlane_b32 s35, v245, 10
	v_add_u32_e32 v66, 0x80, v156
	v_pk_mul_f32 v[64:65], v[68:69], v[64:65]
	v_pk_mul_f32 v[68:69], v[72:73], v[60:61]
	v_pk_mul_f32 v[60:61], v[74:75], v[58:59]
	v_cvt_pk_bf16_f32 v58, v62, v63
	v_mov_b64_e32 v[62:63], s[34:35]
	v_ashrrev_i32_e32 v67, 4, v66
	v_mad_i64_i32 v[62:63], s[34:35], v66, s68, v[62:63]
	v_add_u32_e32 v67, 0xffffc000, v67
	v_lshl_add_u64 v[62:63], v[138:139], 1, v[62:63]
	s_and_b64 vcc, exec, s[10:11]
	v_cvt_pk_bf16_f32 v59, v64, v65
	v_cvt_pk_bf16_f32 v60, v60, v61
	v_cvt_pk_bf16_f32 v61, v68, v69
	global_store_dwordx4 v[62:63], v[58:61], off nt
	s_cbranch_vccnz .LBB0_185
	v_lshl_add_u32 v64, s30, 10, v67
	v_ashrrev_i32_e32 v65, 31, v64
	v_lshlrev_b64 v[64:65], 12, v[64:65]
	v_lshl_add_u64 v[64:65], v[206:207], 0, v[64:65]
	global_store_dwordx4 v[64:65], v[58:61], off nt
.LBB0_185:
	v_cvt_f32_i32_e32 v51, v51
	v_cvt_f32_i32_e32 v53, v53
	v_cvt_f32_i32_e32 v52, v52
	v_cvt_f32_i32_e32 v50, v50
	v_cvt_f32_i32_e32 v55, v55
	v_cvt_f32_i32_e32 v54, v54
	v_cvt_f32_i32_e32 v57, v57
	v_cvt_f32_i32_e32 v56, v56
	v_mov_b32_e32 v155, v154
	v_mov_b32_e32 v58, v154
	v_mov_b32_e32 v59, v154
	v_pk_mul_f32 v[60:61], v[58:59], v[124:125]
	v_pk_mul_f32 v[58:59], v[58:59], v[122:123]
	v_pk_mul_f32 v[68:69], v[154:155], v[128:129]
	v_pk_mul_f32 v[64:65], v[154:155], v[126:127]
	v_pk_mul_f32 v[58:59], v[58:59], v[52:53]
	v_pk_mul_f32 v[52:53], v[68:69], v[50:51]
	s_and_b64 vcc, exec, s[10:11]
	v_pk_mul_f32 v[56:57], v[60:61], v[56:57]
	v_pk_mul_f32 v[54:55], v[64:65], v[54:55]
	s_nop 0
	v_cvt_pk_bf16_f32 v50, v54, v55
	v_cvt_pk_bf16_f32 v51, v56, v57
	v_cvt_pk_bf16_f32 v52, v52, v53
	v_cvt_pk_bf16_f32 v53, v58, v59
	global_store_dwordx4 v[62:63], v[50:53], off offset:256 nt
	s_cbranch_vccnz .LBB0_187
	v_add_u32_e32 v54, v67, v118
	v_ashrrev_i32_e32 v55, 31, v54
	v_lshlrev_b64 v[54:55], 12, v[54:55]
	v_lshl_add_u64 v[54:55], v[206:207], 0, v[54:55]
	global_store_dwordx4 v[54:55], v[50:53], off nt
.LBB0_187:
	v_cvt_f32_i32_e32 v47, v47
	v_cvt_f32_i32_e32 v46, v46
	v_cvt_f32_i32_e32 v49, v49
	v_cvt_f32_i32_e32 v48, v48
	v_cvt_f32_i32_e32 v43, v43
	v_cvt_f32_i32_e32 v45, v45
	v_cvt_f32_i32_e32 v44, v44
	v_cvt_f32_i32_e32 v42, v42
	v_pk_mul_f32 v[54:55], v[152:153], v[150:151] op_sel_hi:[0,1]
	v_readlane_b32 s34, v245, 9
	v_pk_mul_f32 v[52:53], v[152:153], v[148:149] op_sel_hi:[0,1]
	v_pk_mul_f32 v[56:57], v[152:153], v[144:145] op_sel_hi:[0,1]
	v_pk_mul_f32 v[58:59], v[152:153], v[146:147] op_sel_hi:[0,1]
	v_pk_mul_f32 v[46:47], v[54:55], v[46:47]
	v_readlane_b32 s35, v245, 10
	v_or_b32_e32 v51, 16, v66
	v_pk_mul_f32 v[48:49], v[52:53], v[48:49]
	v_pk_mul_f32 v[52:53], v[56:57], v[44:45]
	v_pk_mul_f32 v[44:45], v[58:59], v[42:43]
	v_cvt_pk_bf16_f32 v42, v46, v47
	v_mov_b64_e32 v[46:47], s[34:35]
	v_ashrrev_i32_e32 v50, 4, v51
	v_mad_i64_i32 v[46:47], s[34:35], v51, s68, v[46:47]
	v_add_u32_e32 v50, 0xffffc000, v50
	v_lshl_add_u64 v[46:47], v[138:139], 1, v[46:47]
	s_and_b64 vcc, exec, s[10:11]
	v_cvt_pk_bf16_f32 v43, v48, v49
	v_cvt_pk_bf16_f32 v44, v44, v45
	v_cvt_pk_bf16_f32 v45, v52, v53
	global_store_dwordx4 v[46:47], v[42:45], off nt
	s_cbranch_vccnz .LBB0_189
	v_lshl_add_u32 v48, s30, 10, v50
	v_ashrrev_i32_e32 v49, 31, v48
	v_lshlrev_b64 v[48:49], 12, v[48:49]
	v_lshl_add_u64 v[48:49], v[206:207], 0, v[48:49]
	global_store_dwordx4 v[48:49], v[42:45], off nt
;     __device__ __forceinline__ void operator()(const f32x4 (&acc)[2][2][4][2], const Unit& u, int wr, int wc, int fr, int fq) const {
;     ...
;         for (int kb = 0; kb < 8; ++kb) { const int ai = kb >> 2, m = kb & 3;
;             if (kb < 7) EPB_LOAD(kb + 1);
;             { const int row = row0 + ai * HALF + m * 16; float rmx = 0.f;
; #pragma unroll
;                 for (int bj = 0; bj < 2; ++bj) { const int col = col0 + bj * HALF; f32x4 v0 = acc[ai][bj][m][0], v1 = acc[ai][bj][m][1];
;                     if (QI8) { const f32x4 c0 = cb[bj][0] * ra[ai][m], c1 = cb[bj][1] * ra[ai][m]; const i32x4 i0 = __builtin_bit_cast(i32x4, v0), i1 = __builtin_bit_cast(i32x4, v1);
;                         v0 = (f32x4){(float)i0[0], (float)i0[1], (float)i0[2], (float)i0[3]} * c0; v1 = (f32x4){(float)i1[0], (float)i1[1], (float)i1[2], (float)i1[3]} * c1; }
;                     else if (MODE == 0) { v0 = v0 * tsc; v1 = v1 * tsc; }
;                     if (!QI8 && MODE == 1) { v0 = v0 * cb[bj][0]; v1 = v1 * cb[bj][1]; }
;                     if (MODE == 2 || MODE == 3) { const u32x4 g = gq[kb & 1][bj];
;                         f32x4 g0 = {sigmoidf_(bflo(g.x)), sigmoidf_(bfhi(g.x)), sigmoidf_(bflo(g.y)), sigmoidf_(bfhi(g.y))};
;                         f32x4 g1 = {sigmoidf_(bflo(g.z)), sigmoidf_(bfhi(g.z)), sigmoidf_(bflo(g.w)), sigmoidf_(bfhi(g.w))};
;                         v0 = v0 * g0; v1 = v1 * g1;
;                         if (MODE == 3) { const u32x4 q = aq[kb & 1][bj];
;                             v0 = v0 + (f32x4){bflo(q.x), bfhi(q.x), bflo(q.y), bfhi(q.y)}; v1 = v1 + (f32x4){bflo(q.z), bfhi(q.z), bflo(q.w), bfhi(q.w)}; } }
;                     if (MODE == 4) { v0 = v0 + rs[kb & 1][bj][0]; v1 = v1 + rs[kb & 1][bj][1]; }
;                     if (MODE == 5) { const u32x4 c = gq[kb & 1][bj], q = aq[kb & 1][bj];
;                         v0 = (f32x4){bflo(c.x) + sigmoidf_(v0[0]) * bflo(q.x), bfhi(c.x) + sigmoidf_(v0[1]) * bfhi(q.x), bflo(c.y) + sigmoidf_(v0[2]) * bflo(q.y), bfhi(c.y) + sigmoidf_(v0[3]) * bfhi(q.y)};
;                         v1 = (f32x4){bflo(c.z) + sigmoidf_(v1[0]) * bflo(q.z), bfhi(c.z) + sigmoidf_(v1[1]) * bfhi(q.z), bflo(c.w) + sigmoidf_(v1[2]) * bflo(q.w), bfhi(c.w) + sigmoidf_(v1[3]) * bfhi(q.w)}; }
;                     u32x4 w; w.x = cvtpk(v0[0], v0[1]); w.y = cvtpk(v0[2], v0[3]); w.z = cvtpk(v1[0], v1[1]); w.w = cvtpk(v1[2], v1[3]);
.LBB0_189:
	v_cvt_f32_i32_e32 v35, v35
	v_cvt_f32_i32_e32 v37, v37
	v_cvt_f32_i32_e32 v36, v36
	v_cvt_f32_i32_e32 v34, v34
	v_cvt_f32_i32_e32 v39, v39
	v_cvt_f32_i32_e32 v38, v38
	v_cvt_f32_i32_e32 v41, v41
	v_cvt_f32_i32_e32 v40, v40
	v_mov_b32_e32 v153, v152
	v_mov_b32_e32 v42, v152
	v_mov_b32_e32 v43, v152
	v_pk_mul_f32 v[44:45], v[42:43], v[124:125]
	v_pk_mul_f32 v[42:43], v[42:43], v[122:123]
	v_pk_mul_f32 v[52:53], v[152:153], v[128:129]
	v_pk_mul_f32 v[48:49], v[152:153], v[126:127]
	v_pk_mul_f32 v[42:43], v[42:43], v[36:37]
	v_pk_mul_f32 v[36:37], v[52:53], v[34:35]
	s_and_b64 vcc, exec, s[10:11]
	v_pk_mul_f32 v[40:41], v[44:45], v[40:41]
	v_pk_mul_f32 v[38:39], v[48:49], v[38:39]
	s_nop 0
	v_cvt_pk_bf16_f32 v34, v38, v39
	v_cvt_pk_bf16_f32 v35, v40, v41
	v_cvt_pk_bf16_f32 v36, v36, v37
	v_cvt_pk_bf16_f32 v37, v42, v43
	global_store_dwordx4 v[46:47], v[34:37], off offset:256 nt
	s_cbranch_vccnz .LBB0_191
	v_add_u32_e32 v38, v50, v118
	v_ashrrev_i32_e32 v39, 31, v38
	v_lshlrev_b64 v[38:39], 12, v[38:39]
	v_lshl_add_u64 v[38:39], v[206:207], 0, v[38:39]
	global_store_dwordx4 v[38:39], v[34:37], off nt
.LBB0_191:
	v_cvt_f32_i32_e32 v31, v31
	v_cvt_f32_i32_e32 v30, v30
	v_cvt_f32_i32_e32 v33, v33
	v_cvt_f32_i32_e32 v32, v32
	v_cvt_f32_i32_e32 v27, v27
	v_cvt_f32_i32_e32 v29, v29
	v_cvt_f32_i32_e32 v28, v28
	v_cvt_f32_i32_e32 v26, v26
	v_pk_mul_f32 v[38:39], v[142:143], v[150:151] op_sel_hi:[0,1]
	v_readlane_b32 s34, v245, 9
	v_pk_mul_f32 v[36:37], v[142:143], v[148:149] op_sel_hi:[0,1]
	v_pk_mul_f32 v[40:41], v[142:143], v[144:145] op_sel_hi:[0,1]
	v_pk_mul_f32 v[42:43], v[142:143], v[146:147] op_sel_hi:[0,1]
	v_pk_mul_f32 v[30:31], v[38:39], v[30:31]
	v_readlane_b32 s35, v245, 10
	v_or_b32_e32 v35, 32, v66
	v_pk_mul_f32 v[32:33], v[36:37], v[32:33]
	v_pk_mul_f32 v[36:37], v[40:41], v[28:29]
	v_pk_mul_f32 v[28:29], v[42:43], v[26:27]
	v_cvt_pk_bf16_f32 v26, v30, v31
	v_mov_b64_e32 v[30:31], s[34:35]
	v_ashrrev_i32_e32 v34, 4, v35
	v_mad_i64_i32 v[30:31], s[34:35], v35, s68, v[30:31]
	v_add_u32_e32 v34, 0xffffc000, v34
	v_lshl_add_u64 v[30:31], v[138:139], 1, v[30:31]
	s_and_b64 vcc, exec, s[10:11]
	v_cvt_pk_bf16_f32 v27, v32, v33
	v_cvt_pk_bf16_f32 v28, v28, v29
	v_cvt_pk_bf16_f32 v29, v36, v37
	global_store_dwordx4 v[30:31], v[26:29], off nt
	s_cbranch_vccnz .LBB0_193
	v_lshl_add_u32 v32, s30, 10, v34
	v_ashrrev_i32_e32 v33, 31, v32
	v_lshlrev_b64 v[32:33], 12, v[32:33]
	v_lshl_add_u64 v[32:33], v[206:207], 0, v[32:33]
	global_store_dwordx4 v[32:33], v[26:29], off nt
.LBB0_193:
	v_cvt_f32_i32_e32 v19, v19
	v_cvt_f32_i32_e32 v21, v21
	v_cvt_f32_i32_e32 v20, v20
	v_cvt_f32_i32_e32 v18, v18
	v_cvt_f32_i32_e32 v23, v23
	v_cvt_f32_i32_e32 v22, v22
	v_cvt_f32_i32_e32 v25, v25
	v_cvt_f32_i32_e32 v24, v24
	v_mov_b32_e32 v143, v142
	v_mov_b32_e32 v26, v142
	v_mov_b32_e32 v27, v142
	v_pk_mul_f32 v[28:29], v[26:27], v[124:125]
	v_pk_mul_f32 v[26:27], v[26:27], v[122:123]
	v_pk_mul_f32 v[36:37], v[142:143], v[128:129]
	v_pk_mul_f32 v[32:33], v[142:143], v[126:127]
	v_pk_mul_f32 v[26:27], v[26:27], v[20:21]
	v_pk_mul_f32 v[20:21], v[36:37], v[18:19]
	s_and_b64 vcc, exec, s[10:11]
	v_pk_mul_f32 v[24:25], v[28:29], v[24:25]
	v_pk_mul_f32 v[22:23], v[32:33], v[22:23]
	s_nop 0
	v_cvt_pk_bf16_f32 v18, v22, v23
	v_cvt_pk_bf16_f32 v19, v24, v25
	v_cvt_pk_bf16_f32 v20, v20, v21
	v_cvt_pk_bf16_f32 v21, v26, v27
	global_store_dwordx4 v[30:31], v[18:21], off offset:256 nt
	s_cbranch_vccnz .LBB0_195
	v_add_u32_e32 v22, v34, v118
	v_ashrrev_i32_e32 v23, 31, v22
	v_lshlrev_b64 v[22:23], 12, v[22:23]
	v_lshl_add_u64 v[22:23], v[206:207], 0, v[22:23]
	global_store_dwordx4 v[22:23], v[18:21], off nt
.LBB0_195:
	v_cvt_f32_i32_e32 v15, v15
	v_cvt_f32_i32_e32 v14, v14
	v_cvt_f32_i32_e32 v17, v17
	v_cvt_f32_i32_e32 v16, v16
	v_cvt_f32_i32_e32 v11, v11
	v_cvt_f32_i32_e32 v13, v13
	v_cvt_f32_i32_e32 v12, v12
	v_cvt_f32_i32_e32 v10, v10
	v_pk_mul_f32 v[22:23], v[140:141], v[150:151] op_sel_hi:[0,1]
	v_readlane_b32 s34, v245, 9
	v_pk_mul_f32 v[20:21], v[140:141], v[148:149] op_sel_hi:[0,1]
	v_pk_mul_f32 v[24:25], v[140:141], v[144:145] op_sel_hi:[0,1]
	v_pk_mul_f32 v[26:27], v[140:141], v[146:147] op_sel_hi:[0,1]
	v_pk_mul_f32 v[14:15], v[22:23], v[14:15]
	v_readlane_b32 s35, v245, 10
	v_or_b32_e32 v19, 48, v66
	v_pk_mul_f32 v[16:17], v[20:21], v[16:17]
	v_pk_mul_f32 v[20:21], v[24:25], v[12:13]
	v_pk_mul_f32 v[12:13], v[26:27], v[10:11]
	v_cvt_pk_bf16_f32 v10, v14, v15
	v_mov_b64_e32 v[14:15], s[34:35]
	v_ashrrev_i32_e32 v18, 4, v19
	v_mad_i64_i32 v[14:15], s[34:35], v19, s68, v[14:15]
	v_add_u32_e32 v18, 0xffffc000, v18
	v_lshl_add_u64 v[14:15], v[138:139], 1, v[14:15]
	s_and_b64 vcc, exec, s[10:11]
	v_cvt_pk_bf16_f32 v11, v16, v17
	v_cvt_pk_bf16_f32 v12, v12, v13
	v_cvt_pk_bf16_f32 v13, v20, v21
	global_store_dwordx4 v[14:15], v[10:13], off nt
	s_cbranch_vccnz .LBB0_197
	v_lshl_add_u32 v16, s30, 10, v18
	v_ashrrev_i32_e32 v17, 31, v16
	v_lshlrev_b64 v[16:17], 12, v[16:17]
	v_lshl_add_u64 v[16:17], v[206:207], 0, v[16:17]
	global_store_dwordx4 v[16:17], v[10:13], off nt
.LBB0_197:
	v_cvt_f32_i32_e32 v3, v3
	v_cvt_f32_i32_e32 v5, v5
	v_cvt_f32_i32_e32 v4, v4
	v_cvt_f32_i32_e32 v2, v2
	v_cvt_f32_i32_e32 v7, v7
	v_cvt_f32_i32_e32 v6, v6
	v_cvt_f32_i32_e32 v9, v9
	v_cvt_f32_i32_e32 v8, v8
	v_mov_b32_e32 v141, v140
	v_mov_b32_e32 v10, v140
	v_mov_b32_e32 v11, v140
	v_pk_mul_f32 v[12:13], v[10:11], v[124:125]
	v_pk_mul_f32 v[10:11], v[10:11], v[122:123]
	v_pk_mul_f32 v[20:21], v[140:141], v[128:129]
	v_pk_mul_f32 v[16:17], v[140:141], v[126:127]
	v_pk_mul_f32 v[10:11], v[10:11], v[4:5]
	v_pk_mul_f32 v[4:5], v[20:21], v[2:3]
	s_and_b64 vcc, exec, s[10:11]
	v_pk_mul_f32 v[8:9], v[12:13], v[8:9]
	v_pk_mul_f32 v[6:7], v[16:17], v[6:7]
	s_nop 0
	v_cvt_pk_bf16_f32 v2, v6, v7
	v_cvt_pk_bf16_f32 v3, v8, v9
	v_cvt_pk_bf16_f32 v4, v4, v5
	v_cvt_pk_bf16_f32 v5, v10, v11
	global_store_dwordx4 v[14:15], v[2:5], off offset:256 nt
	s_cbranch_vccnz .LBB0_199
	v_add_u32_e32 v6, v18, v118
	v_ashrrev_i32_e32 v7, 31, v6
	v_lshlrev_b64 v[6:7], 12, v[6:7]
	v_lshl_add_u64 v[6:7], v[206:207], 0, v[6:7]
	global_store_dwordx4 v[6:7], v[2:5], off nt
